# speedup vs baseline: 1.0044x; 1.0044x over previous
_ZN12_GLOBAL__N_18k_bucketEPK15HIP_vector_typeIjLj4EEPKiPiPS1_PKfS9_PDF16_PfSB_:
	s_cmpk_lt_u32 s2, 0x100
	s_mov_b64 s[4:5], -1
	s_cbranch_scc0 .LBB1_27
	s_setprio 3
	s_load_dwordx4 s[8:11], s[0:1], 0x10
	s_load_dwordx2 s[26:27], s[0:1], 0x0
	s_movk_i32 s3, 0xc4
	v_cmp_gt_u32_e32 vcc, s3, v0
	v_mov_b32_e32 v1, 0
	s_and_saveexec_b64 s[4:5], vcc
	s_cbranch_execz .LBB1_3
	s_load_dwordx2 s[6:7], s[0:1], 0x8
	s_mul_i32 s3, s2, 0xc4
	v_mov_b32_e32 v3, 0
	v_add_u32_e32 v2, s3, v0
	s_waitcnt lgkmcnt(0)
	v_lshl_add_u64 v[2:3], v[2:3], 2, s[6:7]
	global_load_dword v1, v[2:3], off
	global_load_dword v4, v[2:3], off offset:784
	v_lshlrev_b32_e32 v2, 2, v0
	v_add_u32_e32 v2, 0x1000, v2
	s_waitcnt vmcnt(0)
	ds_write2_b32 v2, v1, v4 offset1:196
.LBB1_3:
	s_or_b64 exec, exec, s[4:5]
	s_movk_i32 s3, 0x80
	v_cmp_gt_u32_e32 vcc, s3, v0
	s_and_saveexec_b64 s[4:5], vcc
	v_lshlrev_b32_e32 v2, 2, v0
	v_mov_b32_e32 v3, 0
	v_add_u32_e32 v2, 32, v2
	ds_write2st64_b32 v2, v3, v3 offset0:22 offset1:24
	s_or_b64 exec, exec, s[4:5]
	v_add_u32_dpp v1, v1, v1 quad_perm:[1,0,3,2] row_mask:0xf bank_mask:0xf
	s_nop 1
	v_add_u32_dpp v1, v1, v1 quad_perm:[2,3,0,1] row_mask:0xf bank_mask:0xf
	s_nop 1
	v_add_u32_dpp v1, v1, v1 row_half_mirror row_mask:0xf bank_mask:0xf
	s_nop 1
	v_add_u32_dpp v1, v1, v1 row_mirror row_mask:0xf bank_mask:0xf
	s_nop 1
	v_add_u32_dpp v1, v1, v1 row_bcast:15 row_mask:0xa bank_mask:0xf
	s_nop 1
	v_add_u32_dpp v1, v1, v1 row_bcast:31 row_mask:0xc bank_mask:0xf
	v_and_b32_e32 v3, 63, v0
	v_cmp_eq_u32_e32 vcc, 63, v3
	s_and_saveexec_b64 s[4:5], vcc
	s_cbranch_execz .LBB1_7
	v_lshrrev_b32_e32 v2, 6, v0
	v_lshlrev_b32_e32 v2, 2, v2
	ds_write_b32 v2, v1 offset:7200
.LBB1_7:
	s_or_b64 exec, exec, s[4:5]
	v_cmp_eq_u32_e32 vcc, 0, v0
	s_waitcnt lgkmcnt(0)
	s_mov_b64 s[4:5], s[26:27]
	s_barrier
	s_and_saveexec_b64 s[6:7], vcc
	s_cbranch_execz .LBB1_9
	v_mov_b32_e32 v1, 0
	ds_read_b128 v[2:5], v1 offset:7200
	ds_read_b128 v[6:9], v1 offset:7216
	ds_read_b128 v[14:17], v1 offset:7232
	ds_read_b128 v[18:21], v1 offset:7248
	s_waitcnt lgkmcnt(3)
	v_add_u32_e32 v2, v3, v2
	v_add_u32_e32 v2, v4, v2
	v_add_u32_e32 v2, v5, v2
	s_waitcnt lgkmcnt(2)
	v_add_u32_e32 v2, v6, v2
	v_add_u32_e32 v2, v7, v2
	v_add_u32_e32 v2, v8, v2
	v_add_u32_e32 v2, v9, v2
	s_waitcnt lgkmcnt(1)
	v_add_u32_e32 v2, v14, v2
	v_add_u32_e32 v2, v15, v2
	v_add_u32_e32 v2, v16, v2
	v_add_u32_e32 v2, v17, v2
	s_waitcnt lgkmcnt(0)
	v_add_u32_e32 v2, v18, v2
	v_add_u32_e32 v2, v19, v2
	v_add_u32_e32 v2, v20, v2
	v_add_u32_e32 v2, v21, v2
	ds_write_b32 v1, v2 offset:7264

.LBB1_32:
	s_endpgm
	s_nop 0
	s_nop 0
	s_nop 0
	s_nop 0
	s_nop 0
	s_nop 0
	s_nop 0
	s_nop 0
	s_nop 0
	s_nop 0
	s_nop 0
	s_nop 0
	s_nop 0
	s_nop 0
	s_nop 0
	s_nop 0
	s_nop 0
	s_nop 0
	s_nop 0
	s_nop 0
	s_nop 0
	s_nop 0
	s_nop 0
	s_nop 0
	s_nop 0
	s_nop 0
	s_endpgm

	.amdhsa_kernel _ZN12_GLOBAL__N_18k_bucketEPK15HIP_vector_typeIjLj4EEPKiPiPS1_PKfS9_PDF16_PfSB_
		.amdhsa_group_segment_fixed_size 7268
		.amdhsa_private_segment_fixed_size 0
		.amdhsa_kernarg_size 72
		.amdhsa_user_sgpr_count 2
		.amdhsa_user_sgpr_dispatch_ptr 0
		.amdhsa_user_sgpr_queue_ptr 0
		.amdhsa_user_sgpr_kernarg_segment_ptr 1
		.amdhsa_user_sgpr_dispatch_id 0
		.amdhsa_user_sgpr_kernarg_preload_length 0
		.amdhsa_user_sgpr_kernarg_preload_offset 0
		.amdhsa_user_sgpr_private_segment_size 0
		.amdhsa_uses_dynamic_stack 0
		.amdhsa_enable_private_segment 0
		.amdhsa_system_sgpr_workgroup_id_x 1
		.amdhsa_system_sgpr_workgroup_id_y 0
		.amdhsa_system_sgpr_workgroup_id_z 0
		.amdhsa_system_sgpr_workgroup_info 0
		.amdhsa_system_vgpr_workitem_id 0
		.amdhsa_next_free_vgpr 62
		.amdhsa_next_free_sgpr 28
		.amdhsa_accum_offset 64
		.amdhsa_reserve_vcc 1
		.amdhsa_float_round_mode_32 0
		.amdhsa_float_round_mode_16_64 0
		.amdhsa_float_denorm_mode_32 3
		.amdhsa_float_denorm_mode_16_64 3
		.amdhsa_dx10_clamp 1
		.amdhsa_ieee_mode 1
		.amdhsa_fp16_overflow 0
		.amdhsa_tg_split 0
		.amdhsa_exception_fp_ieee_invalid_op 0
		.amdhsa_exception_fp_denorm_src 0
		.amdhsa_exception_fp_ieee_div_zero 0
		.amdhsa_exception_fp_ieee_overflow 0
		.amdhsa_exception_fp_ieee_underflow 0
		.amdhsa_exception_fp_ieee_inexact 0
		.amdhsa_exception_int_div_zero 0
	.end_amdhsa_kernel

amdhsa.kernels:
  - .agpr_count:     0
    .args:
      - .actual_access:  read_only
        .address_space:  global
        .offset:         0
        .size:           8
        .value_kind:     global_buffer
      - .actual_access:  read_only
        .address_space:  global
        .offset:         8
        .size:           8
        .value_kind:     global_buffer
      - .actual_access:  read_only
        .address_space:  global
        .offset:         16
        .size:           8
        .value_kind:     global_buffer
      - .actual_access:  read_only
        .address_space:  global
        .offset:         24
        .size:           8
        .value_kind:     global_buffer
      - .actual_access:  read_only
        .address_space:  global
        .offset:         32
        .size:           8
        .value_kind:     global_buffer
      - .actual_access:  read_only
        .address_space:  global
        .offset:         40
        .size:           8
        .value_kind:     global_buffer
      - .actual_access:  read_only
        .address_space:  global
        .offset:         48
        .size:           8
        .value_kind:     global_buffer
      - .actual_access:  read_only
        .address_space:  global
        .offset:         56
        .size:           8
        .value_kind:     global_buffer
      - .actual_access:  read_only
        .address_space:  global
        .offset:         64
        .size:           8
        .value_kind:     global_buffer
      - .actual_access:  read_only
        .address_space:  global
        .offset:         72
        .size:           8
        .value_kind:     global_buffer
      - .actual_access:  read_only
        .address_space:  global
        .offset:         80
        .size:           8
        .value_kind:     global_buffer
      - .actual_access:  read_only
        .address_space:  global
        .offset:         88
        .size:           8
        .value_kind:     global_buffer
      - .actual_access:  write_only
        .address_space:  global
        .offset:         96
        .size:           8
        .value_kind:     global_buffer
      - .actual_access:  write_only
        .address_space:  global
        .offset:         104
        .size:           8
        .value_kind:     global_buffer
      - .actual_access:  write_only
        .address_space:  global
        .offset:         112
        .size:           8
        .value_kind:     global_buffer
      - .actual_access:  write_only
        .address_space:  global
        .offset:         120
        .size:           8
        .value_kind:     global_buffer
      - .actual_access:  write_only
        .address_space:  global
        .offset:         128
        .size:           8
        .value_kind:     global_buffer
      - .actual_access:  write_only
        .address_space:  global
        .offset:         136
        .size:           8
        .value_kind:     global_buffer
      - .actual_access:  read_only
        .address_space:  global
        .offset:         144
        .size:           8
        .value_kind:     global_buffer
      - .actual_access:  read_only
        .address_space:  global
        .offset:         152
        .size:           8
        .value_kind:     global_buffer
      - .actual_access:  read_only
        .address_space:  global
        .offset:         160
        .size:           8
        .value_kind:     global_buffer
      - .actual_access:  write_only
        .address_space:  global
        .offset:         168
        .size:           8
        .value_kind:     global_buffer
    .group_segment_fixed_size: 4272
    .kernarg_segment_align: 8
    .kernarg_segment_size: 176
    .language:       OpenCL C
    .language_version:
      - 2
      - 0
    .max_flat_workgroup_size: 256
    .name:           _ZN12_GLOBAL__N_16k_prepEPKfPKiS1_S1_S1_S1_S1_S1_S1_S1_S1_S1_P15HIP_vector_typeIjLj4EEPiPfPDF16_S9_S9_S1_S1_S1_S8_
    .private_segment_fixed_size: 0
    .sgpr_count:     30
    .sgpr_spill_count: 0
    .symbol:         _ZN12_GLOBAL__N_16k_prepEPKfPKiS1_S1_S1_S1_S1_S1_S1_S1_S1_S1_P15HIP_vector_typeIjLj4EEPiPfPDF16_S9_S9_S1_S1_S1_S8_.kd
    .uniform_work_group_size: 1
    .uses_dynamic_stack: false
    .vgpr_count:     144
    .vgpr_spill_count: 0
    .wavefront_size: 64
  - .agpr_count:     0
    .args:
      - .actual_access:  read_only
        .address_space:  global
        .offset:         0
        .size:           8
        .value_kind:     global_buffer
      - .actual_access:  read_only
        .address_space:  global
        .offset:         8
        .size:           8
        .value_kind:     global_buffer
      - .actual_access:  write_only
        .address_space:  global
        .offset:         16
        .size:           8
        .value_kind:     global_buffer
      - .actual_access:  write_only
        .address_space:  global
        .offset:         24
        .size:           8
        .value_kind:     global_buffer
      - .actual_access:  read_only
        .address_space:  global
        .offset:         32
        .size:           8
        .value_kind:     global_buffer
      - .actual_access:  read_only
        .address_space:  global
        .offset:         40
        .size:           8
        .value_kind:     global_buffer
      - .actual_access:  write_only
        .address_space:  global
        .offset:         48
        .size:           8
        .value_kind:     global_buffer
      - .actual_access:  write_only
        .address_space:  global
        .offset:         56
        .size:           8
        .value_kind:     global_buffer
      - .actual_access:  write_only
        .address_space:  global
        .offset:         64
        .size:           8
        .value_kind:     global_buffer
    .group_segment_fixed_size: 7268
    .kernarg_segment_align: 8
    .kernarg_segment_size: 72
    .language:       OpenCL C
    .language_version:
      - 2
      - 0
    .max_flat_workgroup_size: 1024
    .name:           _ZN12_GLOBAL__N_18k_bucketEPK15HIP_vector_typeIjLj4EEPKiPiPS1_PKfS9_PDF16_PfSB_
    .private_segment_fixed_size: 0
    .sgpr_count:     34
    .sgpr_spill_count: 0
    .symbol:         _ZN12_GLOBAL__N_18k_bucketEPK15HIP_vector_typeIjLj4EEPKiPiPS1_PKfS9_PDF16_PfSB_.kd
    .uniform_work_group_size: 1
    .uses_dynamic_stack: false
    .vgpr_count:     62
    .vgpr_spill_count: 0
    .wavefront_size: 64
  - .agpr_count:     0
    .args:
      - .actual_access:  read_only
        .address_space:  global
        .offset:         0
        .size:           8
        .value_kind:     global_buffer
      - .actual_access:  read_only
        .address_space:  global
        .offset:         8
        .size:           8
        .value_kind:     global_buffer
      - .actual_access:  read_only
        .address_space:  global
        .offset:         16
        .size:           8
        .value_kind:     global_buffer
      - .actual_access:  read_only
        .address_space:  global
        .offset:         24
        .size:           8
        .value_kind:     global_buffer
      - .actual_access:  read_only
        .address_space:  global
        .offset:         32
        .size:           8
        .value_kind:     global_buffer
      - .actual_access:  read_only
        .address_space:  global
        .offset:         40
        .size:           8
        .value_kind:     global_buffer
      - .actual_access:  read_only
        .address_space:  global
        .offset:         48
        .size:           8
        .value_kind:     global_buffer
      - .actual_access:  read_only
        .address_space:  global
        .offset:         56
        .size:           8
        .value_kind:     global_buffer
      - .actual_access:  read_only
        .address_space:  global
        .offset:         64
        .size:           8
        .value_kind:     global_buffer
      - .actual_access:  read_only
        .address_space:  global
        .offset:         72
        .size:           8
        .value_kind:     global_buffer
      - .actual_access:  write_only
        .address_space:  global
        .offset:         80
        .size:           8
        .value_kind:     global_buffer
      - .actual_access:  write_only
        .address_space:  global
        .offset:         88
        .size:           8
        .value_kind:     global_buffer
      - .actual_access:  write_only
        .address_space:  global
        .offset:         96
        .size:           8
        .value_kind:     global_buffer
      - .actual_access:  read_only
        .address_space:  global
        .offset:         104
        .size:           8
        .value_kind:     global_buffer
    .group_segment_fixed_size: 25216
    .kernarg_segment_align: 8
    .kernarg_segment_size: 112
    .language:       OpenCL C
    .language_version:
      - 2
      - 0
    .max_flat_workgroup_size: 256
    .name:           _ZN12_GLOBAL__N_18k_layer1EPKDF16_PKfS3_PKiPK15HIP_vector_typeIjLj4EES1_S3_S1_S3_S3_PDF16_PfSB_S3_
    .private_segment_fixed_size: 0
    .sgpr_count:     106
    .sgpr_spill_count: 0
    .symbol:         _ZN12_GLOBAL__N_18k_layer1EPKDF16_PKfS3_PKiPK15HIP_vector_typeIjLj4EES1_S3_S1_S3_S3_PDF16_PfSB_S3_.kd
    .uniform_work_group_size: 1
    .uses_dynamic_stack: false
    .vgpr_count:     96
    .vgpr_spill_count: 0
    .wavefront_size: 64
  - .agpr_count:     0
    .args:
      - .actual_access:  read_only
        .address_space:  global
        .offset:         0
        .size:           8
        .value_kind:     global_buffer
      - .actual_access:  read_only
        .address_space:  global
        .offset:         8
        .size:           8
        .value_kind:     global_buffer
      - .actual_access:  read_only
        .address_space:  global
        .offset:         16
        .size:           8
        .value_kind:     global_buffer
      - .actual_access:  read_only
        .address_space:  global
        .offset:         24
        .size:           8
        .value_kind:     global_buffer
      - .actual_access:  read_only
        .address_space:  global
        .offset:         32
        .size:           8
        .value_kind:     global_buffer
      - .actual_access:  read_only
        .address_space:  global
        .offset:         40
        .size:           8
        .value_kind:     global_buffer
      - .actual_access:  read_only
        .address_space:  global
        .offset:         48
        .size:           8
        .value_kind:     global_buffer
      - .actual_access:  write_only
        .address_space:  global
        .offset:         56
        .size:           8
        .value_kind:     global_buffer
    .group_segment_fixed_size: 6144
    .kernarg_segment_align: 8
    .kernarg_segment_size: 64
    .language:       OpenCL C
    .language_version:
      - 2
      - 0
    .max_flat_workgroup_size: 256
    .name:           _ZN12_GLOBAL__N_18k_layer2EPKDF16_PKfS3_PKiPK15HIP_vector_typeIjLj4EES3_S3_PDF16_
    .private_segment_fixed_size: 0
    .sgpr_count:     42
    .sgpr_spill_count: 0
    .symbol:         _ZN12_GLOBAL__N_18k_layer2EPKDF16_PKfS3_PKiPK15HIP_vector_typeIjLj4EES3_S3_PDF16_.kd
    .uniform_work_group_size: 1
    .uses_dynamic_stack: false
    .vgpr_count:     70
    .vgpr_spill_count: 0
    .wavefront_size: 64
  - .agpr_count:     0
    .args:
      - .actual_access:  read_only
        .address_space:  global
        .offset:         0
        .size:           8
        .value_kind:     global_buffer
      - .actual_access:  read_only
        .address_space:  global
        .offset:         8
        .size:           8
        .value_kind:     global_buffer
      - .actual_access:  read_only
        .address_space:  global
        .offset:         16
        .size:           8
        .value_kind:     global_buffer
      - .actual_access:  read_only
        .address_space:  global
        .offset:         24
        .size:           8
        .value_kind:     global_buffer
      - .actual_access:  read_only
        .address_space:  global
        .offset:         32
        .size:           8
        .value_kind:     global_buffer
      - .actual_access:  read_only
        .address_space:  global
        .offset:         40
        .size:           8
        .value_kind:     global_buffer
      - .actual_access:  write_only
        .address_space:  global
        .offset:         48
        .size:           8
        .value_kind:     global_buffer
    .group_segment_fixed_size: 16384
    .kernarg_segment_align: 8
    .kernarg_segment_size: 56
    .language:       OpenCL C
    .language_version:
      - 2
      - 0
    .max_flat_workgroup_size: 512
    .name:           _ZN12_GLOBAL__N_17k_pairsEPKDF16_PKiS1_PKfS5_S5_Pf
    .private_segment_fixed_size: 0
    .sgpr_count:     46
    .sgpr_spill_count: 0
    .symbol:         _ZN12_GLOBAL__N_17k_pairsEPKDF16_PKiS1_PKfS5_S5_Pf.kd
    .uniform_work_group_size: 1
    .uses_dynamic_stack: false
    .vgpr_count:     78
    .vgpr_spill_count: 0
    .wavefront_size: 64
